# hand-written expert-weight converters (rolling buffers, contiguous permlane-shuffled stores), P2 share 14%, 112 converter CUs in P5, exact counted waits at P4 loop header
# baseline (speedup 1.0000x reference)
; #define SEAM(k) do { if (IN(k) && IN((k) + 1)) xcd_barrier(bar); } while (0)
; #define REP(k) for (int _rep = 0; _rep < ((PROBE_DBL == (k)) ? 2 : 1); ++_rep)
; __device__ __forceinline__ void convert_load(Frame& F, int it, f32x4 (&v)[16]) {
;     const int mat = it / TI_PER_MAT, r = it % TI_PER_MAT, type = mat / NE, e = mat % NE, kb = r >> 3, n4 = (r & 7) * 256 + F.lane * 4;
;     const float* src = F.in[type == 0 ? I_WGATE : (type == 1 ? I_WUP : I_WDOWN)] + (size_t)e * D * D + (size_t)(kb * 16) * D + n4;
; #pragma unroll
;     for (int i = 0; i < 16; ++i) v[i] = __builtin_nontemporal_load((const f32x4*)(src + (size_t)i * D));
; }
; __device__ __forceinline__ void convert_store(Frame& F, int it, const f32x4 (&v)[16]) {
;     const int mat = it / TI_PER_MAT, r = it % TI_PER_MAT, type = mat / NE, e = mat % NE, kb = r >> 3, n4 = (r & 7) * 256 + F.lane * 4;
;     unsigned char* dst = F.ws + (type == 0 ? WS_WG : (type == 1 ? WS_WU : WS_WD)) + (size_t)e * D * D + ((size_t)kb * D + n4) * 16;
; #pragma unroll
;     for (int nn = 0; nn < 4; ++nn)
;         *(u32x4*)(dst + nn * 16) = (u32x4){pk_fp8x4(v[0][nn] * W8_SCALE, v[1][nn] * W8_SCALE, v[2][nn] * W8_SCALE, v[3][nn] * W8_SCALE), pk_fp8x4(v[4][nn] * W8_SCALE, v[5][nn] * W8_SCALE, v[6][nn] * W8_SCALE, v[7][nn] * W8_SCALE),
;                                           pk_fp8x4(v[8][nn] * W8_SCALE, v[9][nn] * W8_SCALE, v[10][nn] * W8_SCALE, v[11][nn] * W8_SCALE), pk_fp8x4(v[12][nn] * W8_SCALE, v[13][nn] * W8_SCALE, v[14][nn] * W8_SCALE, v[15][nn] * W8_SCALE)};
; }
; __device__ __forceinline__ void convert_experts(Frame& F, int gw, int NGW, int it0, int it1) {
;     f32x4 A[16], B[16];
;     for (int it = it0 + gw; it < it1; it += 2 * NGW) {
;         const int i2 = it + NGW; const bool h2 = i2 < it1;
;         convert_load(F, it, A); convert_load(F, h2 ? i2 : it, B); __builtin_amdgcn_sched_barrier(0);
; __global__ void __launch_bounds__(512, 2) fwd_kernel(Args args) {
;     ...
;     if (IN(2)) REP(2) { const int gconv = (F.G > 2 * NCONV_WG) ? NCONV_WG : 0, ggemm = F.G - gconv;
;                  if (F.bid < ggemm) { InProj S{D, (const char*)WSP(bf16_t, WS_HM), (const char*)WSP(bf16_t, WS_WIN), WSP(bf16_t, WS_P), ggemm, F.bid}; pg8::gemm_phase(F.lds, S); }
;                  else if (PROBE_DBL != 2 || _rep == 0) convert_experts(F, (F.bid - ggemm) * 8 + F.wave, gconv * 8, 0, ti_early(F.G)); } SEAM(2);
.LBB0_199:
	s_cmp_lt_i32 s68, 3
	s_cselect_b64 s[0:1], -1, 0
	s_and_b64 s[2:3], s[0:1], s[4:5]
	s_andn2_b64 vcc, exec, s[2:3]
	s_cbranch_vccnz .LBB0_227
	s_cmp_gt_i32 s79, 40
	s_cselect_b64 s[2:3], -1, 0
	s_and_b64 s[4:5], s[2:3], exec
	s_cselect_b32 s6, 20, 0
	s_sub_i32 s26, s79, s6
	s_cmp_ge_i32 s80, s26
	s_mov_b64 s[4:5], -1
	s_cbranch_scc0 .LBB0_207
	s_and_b64 s[2:3], s[2:3], exec
	s_cselect_b32 s8, 0x35c2, 0
	s_sub_i32 s2, s80, s26
	s_lshl_b32 s2, s2, 3
	v_readlane_b32 s3, v253, 7
	s_add_i32 s2, s2, s3
	s_cmp_ge_u32 s2, s8
	s_cbranch_scc1 .LBB0_206
	s_lshl_b32 s7, s6, 3
	s_load_dwordx2 s[20:21], s[88:89], 0x98
	s_load_dwordx2 s[22:23], s[88:89], 0xa8
	s_load_dwordx2 s[24:25], s[88:89], 0xb8
	s_add_u32 s28, s86, 0x3000000
	s_addc_u32 s29, s87, 0
	s_add_i32 s9, s8, -1
	s_mov_b32 s10, s2
	s_mov_b32 s11, s2
	s_mov_b32 s30, 0x42800000
	v_lshlrev_b32_e32 v1, 4, v162
	v_and_b32_e32 v2, 15, v162
	v_lshlrev_b32_e32 v2, 6, v2
	v_lshrrev_b32_e32 v3, 4, v162
	v_lshl_add_u32 v2, v3, 4, v2
	v_add_u32_e32 v148, 0x2000, v1
	v_add_u32_e32 v149, 0x4000, v1
	v_add_u32_e32 v150, 0x6000, v1
	v_add_u32_e32 v151, 0x8000, v1
	v_add_u32_e32 v152, 0xa000, v1
	v_add_u32_e32 v153, 0xc000, v1
	v_add_u32_e32 v154, 0xe000, v1
	v_add_u32_e32 v155, 0x10000, v1
	v_add_u32_e32 v156, 0x12000, v1
	v_add_u32_e32 v157, 0x14000, v1
	v_add_u32_e32 v158, 0x16000, v1
	v_add_u32_e32 v228, 0x18000, v1
	v_add_u32_e32 v229, 0x1a000, v1
	v_add_u32_e32 v230, 0x1c000, v1
	v_add_u32_e32 v231, 0x1e000, v1
	s_waitcnt lgkmcnt(0)
	s_min_u32 s12, s10, s9
	s_lshr_b32 s13, s12, 15
	s_and_b32 s14, s12, 0x7fff
	s_lshr_b32 s15, s14, 3
	s_lshl_b32 s15, s15, 17
	s_and_b32 s14, s12, 7
	s_lshl_b32 s14, s14, 10
	s_or_b32 s15, s15, s14
	s_cmp_eq_u32 s13, 0
	s_cselect_b32 s16, s20, s22
	s_cselect_b32 s17, s21, s23
	s_cmp_eq_u32 s13, 2
	s_cselect_b32 s16, s24, s16
	s_cselect_b32 s17, s25, s17
	s_add_u32 s16, s16, s15
	s_addc_u32 s17, s17, 0
	global_load_dwordx4 v[4:7], v1, s[16:17] nt
	global_load_dwordx4 v[8:11], v148, s[16:17] nt
	global_load_dwordx4 v[12:15], v149, s[16:17] nt
	global_load_dwordx4 v[16:19], v150, s[16:17] nt
	global_load_dwordx4 v[20:23], v151, s[16:17] nt
	global_load_dwordx4 v[24:27], v152, s[16:17] nt
	global_load_dwordx4 v[28:31], v153, s[16:17] nt
	global_load_dwordx4 v[32:35], v154, s[16:17] nt
	global_load_dwordx4 v[36:39], v155, s[16:17] nt
	global_load_dwordx4 v[40:43], v156, s[16:17] nt
	global_load_dwordx4 v[44:47], v157, s[16:17] nt
	global_load_dwordx4 v[48:51], v158, s[16:17] nt
	global_load_dwordx4 v[52:55], v228, s[16:17] nt
	global_load_dwordx4 v[56:59], v229, s[16:17] nt
	global_load_dwordx4 v[60:63], v230, s[16:17] nt
	global_load_dwordx4 v[64:67], v231, s[16:17] nt
	s_add_u32 s10, s10, s7
	s_min_u32 s12, s10, s9
	s_lshr_b32 s13, s12, 15
	s_and_b32 s14, s12, 0x7fff
	s_lshr_b32 s15, s14, 3
	s_lshl_b32 s15, s15, 17
	s_and_b32 s14, s12, 7
	s_lshl_b32 s14, s14, 10
	s_or_b32 s15, s15, s14
	s_cmp_eq_u32 s13, 0
	s_cselect_b32 s16, s20, s22
	s_cselect_b32 s17, s21, s23
	s_cmp_eq_u32 s13, 2
	s_cselect_b32 s16, s24, s16
	s_cselect_b32 s17, s25, s17
	s_add_u32 s16, s16, s15
	s_addc_u32 s17, s17, 0
	global_load_dwordx4 v[68:71], v1, s[16:17] nt
	global_load_dwordx4 v[72:75], v148, s[16:17] nt
	global_load_dwordx4 v[76:79], v149, s[16:17] nt
	global_load_dwordx4 v[80:83], v150, s[16:17] nt
	global_load_dwordx4 v[84:87], v151, s[16:17] nt
	global_load_dwordx4 v[88:91], v152, s[16:17] nt
	global_load_dwordx4 v[92:95], v153, s[16:17] nt
	global_load_dwordx4 v[96:99], v154, s[16:17] nt
	global_load_dwordx4 v[100:103], v155, s[16:17] nt
	global_load_dwordx4 v[104:107], v156, s[16:17] nt
	global_load_dwordx4 v[108:111], v157, s[16:17] nt
	global_load_dwordx4 v[112:115], v158, s[16:17] nt
	global_load_dwordx4 v[116:119], v228, s[16:17] nt
	global_load_dwordx4 v[120:123], v229, s[16:17] nt
	global_load_dwordx4 v[124:127], v230, s[16:17] nt
	global_load_dwordx4 v[128:131], v231, s[16:17] nt
	s_add_u32 s10, s10, s7
	s_min_u32 s12, s10, s9
	s_lshr_b32 s13, s12, 15
	s_and_b32 s14, s12, 0x7fff
	s_lshr_b32 s15, s14, 3
	s_lshl_b32 s15, s15, 17
	s_and_b32 s14, s12, 7
	s_lshl_b32 s14, s14, 10
	s_or_b32 s15, s15, s14
	s_cmp_eq_u32 s13, 0
	s_cselect_b32 s16, s20, s22
	s_cselect_b32 s17, s21, s23
	s_cmp_eq_u32 s13, 2
	s_cselect_b32 s16, s24, s16
	s_cselect_b32 s17, s25, s17
	s_add_u32 s16, s16, s15
	s_addc_u32 s17, s17, 0
	global_load_dwordx4 v[164:167], v1, s[16:17] nt
	global_load_dwordx4 v[168:171], v148, s[16:17] nt
	global_load_dwordx4 v[172:175], v149, s[16:17] nt
	global_load_dwordx4 v[176:179], v150, s[16:17] nt
	global_load_dwordx4 v[180:183], v151, s[16:17] nt
	global_load_dwordx4 v[184:187], v152, s[16:17] nt
	global_load_dwordx4 v[188:191], v153, s[16:17] nt
	global_load_dwordx4 v[192:195], v154, s[16:17] nt
	global_load_dwordx4 v[196:199], v155, s[16:17] nt
	global_load_dwordx4 v[200:203], v156, s[16:17] nt
	global_load_dwordx4 v[204:207], v157, s[16:17] nt
	global_load_dwordx4 v[208:211], v158, s[16:17] nt
	global_load_dwordx4 v[212:215], v228, s[16:17] nt
	global_load_dwordx4 v[216:219], v229, s[16:17] nt
	global_load_dwordx4 v[220:223], v230, s[16:17] nt
	global_load_dwordx4 v[224:227], v231, s[16:17] nt
	s_add_u32 s10, s10, s7

; __device__ __forceinline__ unsigned pk_fp8x4(float a, float b, float c, float d) { int w = __builtin_amdgcn_cvt_pk_fp8_f32(a, b, 0, false); w = __builtin_amdgcn_cvt_pk_fp8_f32(c, d, w, true); return (unsigned)w; }
; __device__ __forceinline__ void convert_load(Frame& F, int it, f32x4 (&v)[16]) {
;     const int mat = it / TI_PER_MAT, r = it % TI_PER_MAT, type = mat / NE, e = mat % NE, kb = r >> 3, n4 = (r & 7) * 256 + F.lane * 4;
;     const float* src = F.in[type == 0 ? I_WGATE : (type == 1 ? I_WUP : I_WDOWN)] + (size_t)e * D * D + (size_t)(kb * 16) * D + n4;
; #pragma unroll
;     for (int i = 0; i < 16; ++i) v[i] = __builtin_nontemporal_load((const f32x4*)(src + (size_t)i * D));
; }
; __device__ __forceinline__ void convert_store(Frame& F, int it, const f32x4 (&v)[16]) {
;     const int mat = it / TI_PER_MAT, r = it % TI_PER_MAT, type = mat / NE, e = mat % NE, kb = r >> 3, n4 = (r & 7) * 256 + F.lane * 4;
;     unsigned char* dst = F.ws + (type == 0 ? WS_WG : (type == 1 ? WS_WU : WS_WD)) + (size_t)e * D * D + ((size_t)kb * D + n4) * 16;
; #pragma unroll
;     for (int nn = 0; nn < 4; ++nn)
;         *(u32x4*)(dst + nn * 16) = (u32x4){pk_fp8x4(v[0][nn] * W8_SCALE, v[1][nn] * W8_SCALE, v[2][nn] * W8_SCALE, v[3][nn] * W8_SCALE), pk_fp8x4(v[4][nn] * W8_SCALE, v[5][nn] * W8_SCALE, v[6][nn] * W8_SCALE, v[7][nn] * W8_SCALE),
;                                           pk_fp8x4(v[8][nn] * W8_SCALE, v[9][nn] * W8_SCALE, v[10][nn] * W8_SCALE, v[11][nn] * W8_SCALE), pk_fp8x4(v[12][nn] * W8_SCALE, v[13][nn] * W8_SCALE, v[14][nn] * W8_SCALE, v[15][nn] * W8_SCALE)};
; }
; __device__ __forceinline__ void convert_experts(Frame& F, int gw, int NGW, int it0, int it1) {
;     f32x4 A[16], B[16];
;     for (int it = it0 + gw; it < it1; it += 2 * NGW) {
;         const int i2 = it + NGW; const bool h2 = i2 < it1;
;         convert_load(F, it, A); convert_load(F, h2 ? i2 : it, B); __builtin_amdgcn_sched_barrier(0);
; __device__ __forceinline__ void p4_scan(Frame& F) {
;     ...
;     if (F.bid >= NSCAN) {
;         const int nconv = (F.G - NSCAN) < NCONV_SCAN ? (F.G - NSCAN) : NCONV_SCAN;
;         if (F.bid - NSCAN < nconv) convert_experts(F, (F.bid - NSCAN) * 8 + F.wave, nconv * 8, ti_early(F.G), TI_EXP);
;         return;
.LBB0_721:
	s_and_b64 vcc, exec, s[0:1]
	s_cbranch_vccz .LBB0_728
	s_waitcnt lgkmcnt(0)
	s_min_i32 s0, s79, 0x90
	s_cmp_ge_i32 s80, s0
	s_cbranch_scc1 .LBB0_728
	s_lshl_b32 s1, s80, 3
	v_readlane_b32 s4, v253, 7
	s_add_i32 s4, s1, s4
	s_cmp_gt_i32 s79, 40
	s_cselect_b32 s7, 0x35c2, 0
	s_add_i32 s4, s4, s7
	s_addk_i32 s4, 0xff00
	s_cmp_gt_i32 s4, 0x17fff
	s_cbranch_scc1 .LBB0_728
	s_lshl_b32 s7, s0, 3
	s_addk_i32 s7, 0xff00
	s_mov_b32 s8, 0x18000
	s_load_dwordx2 s[20:21], s[88:89], 0x98
	s_load_dwordx2 s[22:23], s[88:89], 0xa8
	s_load_dwordx2 s[24:25], s[88:89], 0xb8
	s_add_u32 s28, s86, 0x3000000
	s_addc_u32 s29, s87, 0
	s_add_i32 s9, s8, -1
	s_mov_b32 s10, s4
	s_mov_b32 s11, s4
	s_mov_b32 s30, 0x42800000
	v_lshlrev_b32_e32 v1, 4, v162
	v_and_b32_e32 v2, 15, v162
	v_lshlrev_b32_e32 v2, 6, v2
	v_lshrrev_b32_e32 v3, 4, v162
	v_lshl_add_u32 v2, v3, 4, v2
	v_add_u32_e32 v148, 0x2000, v1
	v_add_u32_e32 v149, 0x4000, v1
	v_add_u32_e32 v150, 0x6000, v1
	v_add_u32_e32 v151, 0x8000, v1
	v_add_u32_e32 v152, 0xa000, v1
	v_add_u32_e32 v153, 0xc000, v1
	v_add_u32_e32 v154, 0xe000, v1
	v_add_u32_e32 v155, 0x10000, v1
	v_add_u32_e32 v156, 0x12000, v1
	v_add_u32_e32 v157, 0x14000, v1
	v_add_u32_e32 v158, 0x16000, v1
	v_add_u32_e32 v159, 0x18000, v1
	v_add_u32_e32 v160, 0x1a000, v1
	v_add_u32_e32 v161, 0x1c000, v1
	v_add_u32_e32 v163, 0x1e000, v1
	s_waitcnt lgkmcnt(0)
	s_min_u32 s12, s10, s9
	s_lshr_b32 s13, s12, 15
	s_and_b32 s14, s12, 0x7fff
	s_lshr_b32 s15, s14, 3
	s_lshl_b32 s15, s15, 17
	s_and_b32 s14, s12, 7
	s_lshl_b32 s14, s14, 10
	s_or_b32 s15, s15, s14
	s_cmp_eq_u32 s13, 0
	s_cselect_b32 s16, s20, s22
	s_cselect_b32 s17, s21, s23
	s_cmp_eq_u32 s13, 2
	s_cselect_b32 s16, s24, s16
	s_cselect_b32 s17, s25, s17
	s_add_u32 s16, s16, s15
	s_addc_u32 s17, s17, 0
	global_load_dwordx4 v[4:7], v1, s[16:17] nt
	global_load_dwordx4 v[8:11], v148, s[16:17] nt
	global_load_dwordx4 v[12:15], v149, s[16:17] nt
	global_load_dwordx4 v[16:19], v150, s[16:17] nt
	global_load_dwordx4 v[20:23], v151, s[16:17] nt
	global_load_dwordx4 v[24:27], v152, s[16:17] nt
	global_load_dwordx4 v[28:31], v153, s[16:17] nt
	global_load_dwordx4 v[32:35], v154, s[16:17] nt
	global_load_dwordx4 v[36:39], v155, s[16:17] nt
	global_load_dwordx4 v[40:43], v156, s[16:17] nt
	global_load_dwordx4 v[44:47], v157, s[16:17] nt
	global_load_dwordx4 v[48:51], v158, s[16:17] nt
	global_load_dwordx4 v[52:55], v159, s[16:17] nt
	global_load_dwordx4 v[56:59], v160, s[16:17] nt
	global_load_dwordx4 v[60:63], v161, s[16:17] nt
	global_load_dwordx4 v[64:67], v163, s[16:17] nt
	s_add_u32 s10, s10, s7
